# speedup vs baseline: 1.0068x; 1.0068x over previous
.Lk1_flush:
	s_add_u32 s20, s40, 0x0
	s_addc_u32 s21, s41, 0
	s_add_u32 s22, s20, 0x186a000
	s_addc_u32 s23, s21, 0
	s_add_u32 s24, s22, 0x186a000
	s_addc_u32 s25, s23, 0
	s_add_u32 s26, s24, 0x186a000
	s_addc_u32 s27, s25, 0
	global_store_dword v39, v56, s[20:21] sc1
	global_store_dword v39, v57, s[22:23] sc1
	global_store_dword v39, v58, s[24:25] sc1
	global_store_dword v39, v59, s[26:27] sc1
	s_add_u32 s20, s20, 0x80000
	s_addc_u32 s21, s21, 0
	s_add_u32 s22, s22, 0x80000
	s_addc_u32 s23, s23, 0
	s_add_u32 s24, s24, 0x80000
	s_addc_u32 s25, s25, 0
	s_add_u32 s26, s26, 0x80000
	s_addc_u32 s27, s27, 0
	global_store_dword v39, v60, s[20:21] sc1
	global_store_dword v39, v61, s[22:23] sc1
	global_store_dword v39, v62, s[24:25] sc1
	global_store_dword v39, v63, s[26:27] sc1
	s_add_u32 s20, s20, 0x80000
	s_addc_u32 s21, s21, 0
	s_add_u32 s22, s22, 0x80000
	s_addc_u32 s23, s23, 0
	s_add_u32 s24, s24, 0x80000
	s_addc_u32 s25, s25, 0
	s_add_u32 s26, s26, 0x80000
	s_addc_u32 s27, s27, 0
	global_store_dword v39, v64, s[20:21] sc1
	global_store_dword v39, v65, s[22:23] sc1
	global_store_dword v39, v66, s[24:25] sc1
	global_store_dword v39, v67, s[26:27] sc1
	s_add_u32 s20, s20, 0x80000
	s_addc_u32 s21, s21, 0
	s_add_u32 s22, s22, 0x80000
	s_addc_u32 s23, s23, 0
	s_add_u32 s24, s24, 0x80000
	s_addc_u32 s25, s25, 0
	s_add_u32 s26, s26, 0x80000
	s_addc_u32 s27, s27, 0
	global_store_dword v39, v68, s[20:21] sc1
	global_store_dword v39, v69, s[22:23] sc1
	global_store_dword v39, v70, s[24:25] sc1
	global_store_dword v39, v71, s[26:27] sc1
	s_add_u32 s20, s20, 0x80000
	s_addc_u32 s21, s21, 0
	s_add_u32 s22, s22, 0x80000
	s_addc_u32 s23, s23, 0
	s_add_u32 s24, s24, 0x80000
	s_addc_u32 s25, s25, 0
	s_add_u32 s26, s26, 0x80000
	s_addc_u32 s27, s27, 0
	global_store_dword v39, v72, s[20:21] sc1
	global_store_dword v39, v73, s[22:23] sc1
	global_store_dword v39, v74, s[24:25] sc1
	global_store_dword v39, v75, s[26:27] sc1
	s_add_u32 s20, s20, 0x80000
	s_addc_u32 s21, s21, 0
	s_add_u32 s22, s22, 0x80000
	s_addc_u32 s23, s23, 0
	s_add_u32 s24, s24, 0x80000
	s_addc_u32 s25, s25, 0
	s_add_u32 s26, s26, 0x80000
	s_addc_u32 s27, s27, 0
	global_store_dword v39, v76, s[20:21] sc1
	global_store_dword v39, v77, s[22:23] sc1
	global_store_dword v39, v78, s[24:25] sc1
	global_store_dword v39, v79, s[26:27] sc1
	s_add_u32 s20, s20, 0x80000
	s_addc_u32 s21, s21, 0
	s_add_u32 s22, s22, 0x80000
	s_addc_u32 s23, s23, 0
	s_add_u32 s24, s24, 0x80000
	s_addc_u32 s25, s25, 0
	s_add_u32 s26, s26, 0x80000
	s_addc_u32 s27, s27, 0
	global_store_dword v39, v80, s[20:21] sc1
	global_store_dword v39, v81, s[22:23] sc1
	global_store_dword v39, v82, s[24:25] sc1
	global_store_dword v39, v83, s[26:27] sc1
	s_add_u32 s20, s20, 0x80000
	s_addc_u32 s21, s21, 0
	s_add_u32 s22, s22, 0x80000
	s_addc_u32 s23, s23, 0
	s_add_u32 s24, s24, 0x80000
	s_addc_u32 s25, s25, 0
	s_add_u32 s26, s26, 0x80000
	s_addc_u32 s27, s27, 0
	global_store_dword v39, v84, s[20:21] sc1
	global_store_dword v39, v85, s[22:23] sc1
	global_store_dword v39, v86, s[24:25] sc1
	global_store_dword v39, v87, s[26:27] sc1
	s_add_u32 s20, s20, 0x80000
	s_addc_u32 s21, s21, 0
	s_add_u32 s22, s22, 0x80000
	s_addc_u32 s23, s23, 0
	s_add_u32 s24, s24, 0x80000
	s_addc_u32 s25, s25, 0
	s_add_u32 s26, s26, 0x80000
	s_addc_u32 s27, s27, 0
	global_store_dword v39, v88, s[20:21] sc1
	global_store_dword v39, v89, s[22:23] sc1
	global_store_dword v39, v90, s[24:25] sc1
	global_store_dword v39, v91, s[26:27] sc1
	s_add_u32 s20, s20, 0x80000
	s_addc_u32 s21, s21, 0
	s_add_u32 s22, s22, 0x80000
	s_addc_u32 s23, s23, 0
	s_add_u32 s24, s24, 0x80000
	s_addc_u32 s25, s25, 0
	s_add_u32 s26, s26, 0x80000
	s_addc_u32 s27, s27, 0
	global_store_dword v39, v92, s[20:21] sc1
	global_store_dword v39, v93, s[22:23] sc1
	global_store_dword v39, v94, s[24:25] sc1
	global_store_dword v39, v95, s[26:27] sc1
	s_add_u32 s20, s20, 0x80000
	s_addc_u32 s21, s21, 0
	s_add_u32 s22, s22, 0x80000
	s_addc_u32 s23, s23, 0
	s_add_u32 s24, s24, 0x80000
	s_addc_u32 s25, s25, 0
	s_add_u32 s26, s26, 0x80000
	s_addc_u32 s27, s27, 0
	global_store_dword v39, v96, s[20:21] sc1
	global_store_dword v39, v97, s[22:23] sc1
	global_store_dword v39, v98, s[24:25] sc1
	global_store_dword v39, v99, s[26:27] sc1
	s_add_u32 s20, s20, 0x80000
	s_addc_u32 s21, s21, 0
	s_add_u32 s22, s22, 0x80000
	s_addc_u32 s23, s23, 0
	s_add_u32 s24, s24, 0x80000
	s_addc_u32 s25, s25, 0
	s_add_u32 s26, s26, 0x80000
	s_addc_u32 s27, s27, 0
	global_store_dword v39, v100, s[20:21] sc1
	global_store_dword v39, v101, s[22:23] sc1
	global_store_dword v39, v102, s[24:25] sc1
	global_store_dword v39, v103, s[26:27] sc1
	s_add_u32 s20, s20, 0x80000
	s_addc_u32 s21, s21, 0
	s_add_u32 s22, s22, 0x80000
	s_addc_u32 s23, s23, 0
	s_add_u32 s24, s24, 0x80000
	s_addc_u32 s25, s25, 0
	s_add_u32 s26, s26, 0x80000
	s_addc_u32 s27, s27, 0
	global_store_dword v39, v104, s[20:21] sc1
	global_store_dword v39, v105, s[22:23] sc1
	global_store_dword v39, v106, s[24:25] sc1
	global_store_dword v39, v107, s[26:27] sc1
	s_add_u32 s20, s20, 0x80000
	s_addc_u32 s21, s21, 0
	s_add_u32 s22, s22, 0x80000
	s_addc_u32 s23, s23, 0
	s_add_u32 s24, s24, 0x80000
	s_addc_u32 s25, s25, 0
	s_add_u32 s26, s26, 0x80000
	s_addc_u32 s27, s27, 0
	global_store_dword v39, v108, s[20:21] sc1
	global_store_dword v39, v109, s[22:23] sc1
	global_store_dword v39, v110, s[24:25] sc1
	global_store_dword v39, v111, s[26:27] sc1
	s_add_u32 s20, s20, 0x80000
	s_addc_u32 s21, s21, 0
	s_add_u32 s22, s22, 0x80000
	s_addc_u32 s23, s23, 0
	s_add_u32 s24, s24, 0x80000
	s_addc_u32 s25, s25, 0
	s_add_u32 s26, s26, 0x80000
	s_addc_u32 s27, s27, 0
	global_store_dword v39, v112, s[20:21] sc1
	global_store_dword v39, v113, s[22:23] sc1
	global_store_dword v39, v114, s[24:25] sc1
	global_store_dword v39, v115, s[26:27] sc1
	s_add_u32 s20, s20, 0x80000
	s_addc_u32 s21, s21, 0
	s_add_u32 s22, s22, 0x80000
	s_addc_u32 s23, s23, 0
	s_add_u32 s24, s24, 0x80000
	s_addc_u32 s25, s25, 0
	s_add_u32 s26, s26, 0x80000
	s_addc_u32 s27, s27, 0
	global_store_dword v39, v116, s[20:21] sc1
	global_store_dword v39, v117, s[22:23] sc1
	global_store_dword v39, v118, s[24:25] sc1
	global_store_dword v39, v119, s[26:27] sc1
	s_add_u32 s20, s20, 0x80000
	s_addc_u32 s21, s21, 0
	s_add_u32 s22, s22, 0x80000
	s_addc_u32 s23, s23, 0
	s_add_u32 s24, s24, 0x80000
	s_addc_u32 s25, s25, 0
	s_add_u32 s26, s26, 0x80000
	s_addc_u32 s27, s27, 0
	global_store_dword v39, v120, s[20:21] sc1
	global_store_dword v39, v121, s[22:23] sc1
	global_store_dword v39, v122, s[24:25] sc1
	global_store_dword v39, v123, s[26:27] sc1
	s_add_u32 s20, s20, 0x80000
	s_addc_u32 s21, s21, 0
	s_add_u32 s22, s22, 0x80000
	s_addc_u32 s23, s23, 0
	s_add_u32 s24, s24, 0x80000
	s_addc_u32 s25, s25, 0
	s_add_u32 s26, s26, 0x80000
	s_addc_u32 s27, s27, 0
	global_store_dword v39, v124, s[20:21] sc1
	global_store_dword v39, v125, s[22:23] sc1
	global_store_dword v39, v126, s[24:25] sc1
	global_store_dword v39, v127, s[26:27] sc1
	s_add_u32 s20, s20, 0x80000
	s_addc_u32 s21, s21, 0
	s_add_u32 s22, s22, 0x80000
	s_addc_u32 s23, s23, 0
	s_add_u32 s24, s24, 0x80000
	s_addc_u32 s25, s25, 0
	s_add_u32 s26, s26, 0x80000
	s_addc_u32 s27, s27, 0
	global_store_dword v39, v36, s[20:21] sc1
	global_store_dword v39, v37, s[22:23] sc1
	global_store_dword v39, v45, s[24:25] sc1
	global_store_dword v39, v46, s[26:27] sc1
	s_add_u32 s20, s20, 0x80000
	s_addc_u32 s21, s21, 0
	s_add_u32 s22, s22, 0x80000
	s_addc_u32 s23, s23, 0
	s_add_u32 s24, s24, 0x80000
	s_addc_u32 s25, s25, 0
	s_add_u32 s26, s26, 0x80000
	s_addc_u32 s27, s27, 0
	global_store_dword v39, v53, s[20:21] sc1
	global_store_dword v39, v54, s[22:23] sc1
	global_store_dword v39, v55, s[24:25] sc1
	global_store_dword v39, v1, s[26:27] sc1
	s_add_u32 s20, s20, 0x80000
	s_addc_u32 s21, s21, 0
	s_add_u32 s22, s22, 0x80000
	s_addc_u32 s23, s23, 0
	s_add_u32 s24, s24, 0x80000
	s_addc_u32 s25, s25, 0
	s_add_u32 s26, s26, 0x80000
	s_addc_u32 s27, s27, 0
	ds_read_b128 v[56:59], v38 offset:4096
	ds_read_b128 v[60:63], v38 offset:5120
	ds_read_b128 v[64:67], v38 offset:6144
	ds_read_b128 v[68:71], v38 offset:7168
	s_waitcnt lgkmcnt(0)
	global_store_dword v39, v56, s[20:21] sc1
	global_store_dword v39, v57, s[22:23] sc1
	global_store_dword v39, v58, s[24:25] sc1
	global_store_dword v39, v59, s[26:27] sc1
	s_add_u32 s20, s20, 0x80000
	s_addc_u32 s21, s21, 0
	s_add_u32 s22, s22, 0x80000
	s_addc_u32 s23, s23, 0
	s_add_u32 s24, s24, 0x80000
	s_addc_u32 s25, s25, 0
	s_add_u32 s26, s26, 0x80000
	s_addc_u32 s27, s27, 0
	global_store_dword v39, v60, s[20:21] sc1
	global_store_dword v39, v61, s[22:23] sc1
	global_store_dword v39, v62, s[24:25] sc1
	global_store_dword v39, v63, s[26:27] sc1
	s_add_u32 s20, s20, 0x80000
	s_addc_u32 s21, s21, 0
	s_add_u32 s22, s22, 0x80000
	s_addc_u32 s23, s23, 0
	s_add_u32 s24, s24, 0x80000
	s_addc_u32 s25, s25, 0
	s_add_u32 s26, s26, 0x80000
	s_addc_u32 s27, s27, 0
	global_store_dword v39, v64, s[20:21] sc1
	global_store_dword v39, v65, s[22:23] sc1
	global_store_dword v39, v66, s[24:25] sc1
	global_store_dword v39, v67, s[26:27] sc1
	s_add_u32 s20, s20, 0x80000
	s_addc_u32 s21, s21, 0
	s_add_u32 s22, s22, 0x80000
	s_addc_u32 s23, s23, 0
	s_add_u32 s24, s24, 0x80000
	s_addc_u32 s25, s25, 0
	s_add_u32 s26, s26, 0x80000
	s_addc_u32 s27, s27, 0
	global_store_dword v39, v68, s[20:21] sc1
	global_store_dword v39, v69, s[22:23] sc1
	global_store_dword v39, v70, s[24:25] sc1
	global_store_dword v39, v71, s[26:27] sc1
	v_mul_f32_e32 v40, 0x3c010204, v40
	v_and_b32_e32 v42, 63, v0
	v_lshlrev_b32_e32 v41, 14, v42
	s_mov_b32 s15, s12
	s_lshl_b32 s15, s15, 2
	s_add_u32 s8, s8, s15
	s_addc_u32 s9, s9, 0
	s_add_u32 s15, s29, 24
	v_cmp_gt_u32_e32 vcc, s15, v42
	s_and_saveexec_b64 s[38:39], vcc
	global_store_dword v41, v40, s[8:9]
	s_mov_b64 exec, s[38:39]
	s_lshl_b32 s15, s14, 12
	v_add_u32_e32 v41, s15, v34
	s_barrier
	ds_write_b128 v41, v[2:5]
	ds_write_b128 v41, v[6:9] offset:1024
	ds_write_b128 v41, v[10:13] offset:2048
	ds_write_b128 v41, v[14:17] offset:3072
	s_waitcnt lgkmcnt(0)
	s_barrier
	s_movk_i32 s15, 0x100
	v_cmp_gt_u32_e32 vcc, s15, v0
	s_and_saveexec_b64 s[38:39], vcc
	s_cbranch_execz .Lk1_end
	v_lshlrev_b32_e32 v16, 4, v0
	ds_read_b128 v[2:5], v16
	ds_read_b128 v[18:21], v16 offset:4096
	ds_read_b128 v[22:25], v16 offset:8192
	ds_read_b128 v[26:29], v16 offset:12288
	ds_read_b128 v[30:33], v16 offset:16384
	ds_read_b128 v[34:37], v16 offset:20480
	ds_read_b128 v[38:41], v16 offset:24576
	ds_read_b128 v[42:45], v16 offset:28672
	s_waitcnt lgkmcnt(6)
	v_pk_add_f32 v[2:3], v[2:3], v[18:19]
	v_pk_add_f32 v[4:5], v[4:5], v[20:21]
	s_waitcnt lgkmcnt(5)
	v_pk_add_f32 v[2:3], v[2:3], v[22:23]
	v_pk_add_f32 v[4:5], v[4:5], v[24:25]
	s_waitcnt lgkmcnt(4)
	v_pk_add_f32 v[2:3], v[2:3], v[26:27]
	v_pk_add_f32 v[4:5], v[4:5], v[28:29]
	s_waitcnt lgkmcnt(3)
	v_pk_add_f32 v[2:3], v[2:3], v[30:31]
	v_pk_add_f32 v[4:5], v[4:5], v[32:33]
	s_waitcnt lgkmcnt(2)
	v_pk_add_f32 v[2:3], v[2:3], v[34:35]
	v_pk_add_f32 v[4:5], v[4:5], v[36:37]
	s_waitcnt lgkmcnt(1)
	v_pk_add_f32 v[2:3], v[2:3], v[38:39]
	v_pk_add_f32 v[4:5], v[4:5], v[40:41]
	s_waitcnt lgkmcnt(0)
	v_pk_add_f32 v[2:3], v[2:3], v[42:43]
	v_pk_add_f32 v[4:5], v[4:5], v[44:45]
	s_lshl_b32 s15, s2, 12
	s_add_u32 s10, s10, s15
	s_addc_u32 s11, s11, 0
	global_store_dwordx4 v16, v[2:5], s[10:11]
